# baseline (speedup 1.0000x reference)
.Lsds_dma_done:
	s_load_dwordx4 s[8:11], s[0:1], 0x0
	s_and_b32 s16, s2, 7
	s_bfe_u32 s14, s2, 0x10003
	s_cmp_eq_u32 s14, 0
	s_cselect_b64 s[12:13], -1, 0
	s_and_b64 s[4:5], s[12:13], exec
	s_mul_i32 s3, s16, 0x9600
	v_and_b32_e32 v206, 15, v0
	v_bfe_u32 v207, v0, 6, 2
	s_waitcnt lgkmcnt(0)
	s_cselect_b32 s4, s9, s11
	s_cselect_b32 s5, s8, s10
	s_lshl_b32 s3, s3, 2
	v_bfe_u32 v208, v0, 4, 2
	v_lshl_or_b32 v1, v207, 5, v206
	s_add_u32 s6, s5, s3
	v_lshlrev_b32_e32 v209, 3, v208
	v_mul_u32_u24_e32 v76, 0x12c, v1
	s_addc_u32 s7, s4, 0
	v_add_lshl_u32 v202, v209, v76, 2
	global_load_dwordx4 v[66:69], v202, s[6:7] offset:16
	global_load_dwordx4 v[70:73], v202, s[6:7]
	global_load_dwordx4 v[58:61], v202, s[6:7] offset:144
	global_load_dwordx4 v[62:65], v202, s[6:7] offset:128
	global_load_dwordx4 v[50:53], v202, s[6:7] offset:272
	global_load_dwordx4 v[54:57], v202, s[6:7] offset:256
	global_load_dwordx4 v[42:45], v202, s[6:7] offset:400
	global_load_dwordx4 v[46:49], v202, s[6:7] offset:384
	global_load_dwordx4 v[34:37], v202, s[6:7] offset:528
	global_load_dwordx4 v[38:41], v202, s[6:7] offset:512
	global_load_dwordx4 v[26:29], v202, s[6:7] offset:656
	global_load_dwordx4 v[30:33], v202, s[6:7] offset:640
	global_load_dwordx4 v[18:21], v202, s[6:7] offset:784
	global_load_dwordx4 v[22:25], v202, s[6:7] offset:768
	global_load_dwordx4 v[10:13], v202, s[6:7] offset:912
	global_load_dwordx4 v[14:17], v202, s[6:7] offset:896
	global_load_dwordx4 v[2:5], v202, s[6:7] offset:1040
	global_load_dwordx4 v[6:9], v202, s[6:7] offset:1024
	s_movk_i32 s8, 0x12c
	v_mov_b32_e32 v203, 0
	v_or_b32_e32 v1, 0x120, v209
	v_lshl_add_u64 v[74:75], s[6:7], 0, v[202:203]
	v_cmp_gt_u32_e32 vcc, s8, v1
	v_mov_b32_e32 v210, 0
	v_mov_b32_e32 v211, 0
	v_mov_b32_e32 v212, 0
	v_mov_b32_e32 v230, 0
	v_mov_b32_e32 v231, 0
	v_mov_b32_e32 v232, 0
	v_mov_b32_e32 v233, 0
	v_mov_b32_e32 v234, 0
	v_mov_b32_e32 v235, 0
	v_mov_b32_e32 v236, 0
	v_mov_b32_e32 v237, 0
	v_mov_b32_e32 v238, 0
	v_mov_b32_e32 v239, 0
	v_mov_b32_e32 v240, 0
	v_mov_b32_e32 v241, 0
	v_mov_b32_e32 v242, 0
	v_mov_b32_e32 v243, 0
	v_mov_b32_e32 v244, 0
	v_mov_b32_e32 v245, 0
	s_and_saveexec_b64 s[4:5], vcc
	s_cbranch_execz .LBB1_2
	global_load_dwordx4 v[230:233], v[74:75], off offset:1152

.LBB1_8:
	s_or_b64 exec, exec, s[6:7]
	s_waitcnt vmcnt(0) lgkmcnt(0)
	v_cvt_f16_f32_e32 v210, v230
	v_cvt_f16_f32_e32 v211, v233
	v_cvt_pk_f16_f32 v212, v231, v232
	v_cvt_pk_f16_f32 v203, v234, v235
	v_cvt_pk_f16_f32 v1, v236, v237
	v_cvt_f16_f32_e32 v204, v238
	v_cvt_f16_f32_e32 v213, v241
	v_cvt_pk_f16_f32 v214, v239, v240
	v_cvt_pk_f16_f32 v205, v242, v243
	v_cvt_pk_f16_f32 v202, v244, v245
	s_load_dwordx2 s[8:9], s[0:1], 0x18
	s_load_dwordx4 s[4:7], s[0:1], 0x28
	s_ashr_i32 s0, s2, 1
	s_and_b32 s17, s0, -8
	s_movk_i32 s0, 0x280
	v_cmp_gt_u32_e32 vcc, s0, v0
	s_and_saveexec_b64 s[0:1], vcc
	s_cbranch_execz .LBB1_21
	s_add_u32 s2, s10, s3
	s_addc_u32 s3, s11, 0
	s_mov_b64 s[10:11], 0
	s_movk_i32 s18, 0xffb0
	s_movk_i32 s19, 0x4b
	s_movk_i32 s20, 0x12c
	s_mov_b32 s21, 0x5040100
	s_mov_b32 s22, 0x1c400
	s_movk_i32 s23, 0x7f
	v_mov_b32_e32 v147, v0
	s_branch .LBB1_19
